# attention S-MFMA srcC as inline 0.5 (no per-iteration 16-VGPR constant rebuild), s_nop 6 removed
# speedup vs baseline: 1.0038x; 1.0038x over previous
.LBB0_631:
	v_pk_mul_f32 v[0:1], v[106:107], s[58:59] op_sel_hi:[1,0]
	s_and_b64 s[28:29], s[72:73], exec
	v_cvt_pk_bf16_f32 v118, v0, v1
	v_pk_mul_f32 v[0:1], v[102:103], s[58:59] op_sel_hi:[1,0]
	s_cselect_b32 s4, -2, 0xffffffbe
	v_cvt_pk_bf16_f32 v119, v0, v1
	v_pk_mul_f32 v[0:1], v[36:37], s[58:59] op_sel_hi:[1,0]
	s_add_u32 s28, s27, s12
	v_cvt_pk_bf16_f32 v120, v0, v1
	v_pk_mul_f32 v[0:1], v[32:33], s[58:59] op_sel_hi:[1,0]
	s_addc_u32 s29, 0, 0
	v_cvt_pk_bf16_f32 v121, v0, v1
	v_pk_mul_f32 v[0:1], v[28:29], s[58:59] op_sel_hi:[1,0]
	s_lshr_b64 s[28:29], s[28:29], 1
	v_cvt_pk_bf16_f32 v122, v0, v1
	v_pk_mul_f32 v[0:1], v[30:31], s[58:59] op_sel_hi:[1,0]
	s_mul_i32 s13, s28, 0x220000
	v_cvt_pk_bf16_f32 v123, v0, v1
	v_pk_mul_f32 v[0:1], v[24:25], s[58:59] op_sel_hi:[1,0]
	s_mul_hi_u32 s29, s28, 0x220000
	v_cvt_pk_bf16_f32 v124, v0, v1
	v_pk_mul_f32 v[0:1], v[26:27], s[58:59] op_sel_hi:[1,0]
	s_or_b32 s28, s13, s70
	v_cvt_pk_bf16_f32 v125, v0, v1
	v_pk_mul_f32 v[0:1], v[90:91], s[58:59] op_sel_hi:[1,0]
	v_mov_b32_e32 v32, 0
	v_cvt_pk_bf16_f32 v126, v0, v1
	v_pk_mul_f32 v[0:1], v[38:39], s[58:59] op_sel_hi:[1,0]
	s_mov_b32 s12, 1
	v_cvt_pk_bf16_f32 v127, v0, v1
	v_pk_mul_f32 v[0:1], v[34:35], s[58:59] op_sel_hi:[1,0]
	v_lshl_add_u64 v[194:195], v[188:189], 0, s[28:29]
	v_cvt_pk_bf16_f32 v128, v0, v1
	v_pk_mul_f32 v[0:1], v[18:19], s[58:59] op_sel_hi:[1,0]
	v_mov_b32_e32 v33, v32
	v_cvt_pk_bf16_f32 v129, v0, v1
	v_pk_mul_f32 v[0:1], v[16:17], s[58:59] op_sel_hi:[1,0]
	v_mov_b32_e32 v34, v32
	v_cvt_pk_bf16_f32 v130, v0, v1
	v_pk_mul_f32 v[0:1], v[14:15], s[58:59] op_sel_hi:[1,0]
	v_mov_b32_e32 v35, v32
	v_cvt_pk_bf16_f32 v131, v0, v1
	v_pk_mul_f32 v[0:1], v[12:13], s[58:59] op_sel_hi:[1,0]
	v_mov_b32_e32 v36, v32
	v_cvt_pk_bf16_f32 v132, v0, v1
	v_pk_mul_f32 v[0:1], v[20:21], s[58:59] op_sel_hi:[1,0]
	v_mov_b32_e32 v37, v32
	v_cvt_pk_bf16_f32 v133, v0, v1
	v_pk_mul_f32 v[0:1], v[78:79], s[58:59] op_sel_hi:[1,0]
	v_mov_b32_e32 v38, v32
	v_cvt_pk_bf16_f32 v134, v0, v1
	v_pk_mul_f32 v[0:1], v[74:75], s[58:59] op_sel_hi:[1,0]
	v_mov_b32_e32 v39, v32
	v_cvt_pk_bf16_f32 v135, v0, v1
	v_pk_mul_f32 v[0:1], v[70:71], s[58:59] op_sel_hi:[1,0]
	v_mov_b32_e32 v40, v32
	v_cvt_pk_bf16_f32 v136, v0, v1
	v_pk_mul_f32 v[0:1], v[66:67], s[58:59] op_sel_hi:[1,0]
	v_mov_b32_e32 v41, v32
	v_cvt_pk_bf16_f32 v137, v0, v1
	v_pk_mul_f32 v[0:1], v[56:57], s[58:59] op_sel_hi:[1,0]
	v_mov_b32_e32 v42, v32
	v_cvt_pk_bf16_f32 v138, v0, v1
	v_pk_mul_f32 v[0:1], v[60:61], s[58:59] op_sel_hi:[1,0]
	v_mov_b32_e32 v43, v32
	v_cvt_pk_bf16_f32 v139, v0, v1
	v_pk_mul_f32 v[0:1], v[52:53], s[58:59] op_sel_hi:[1,0]
	v_mov_b32_e32 v48, v32
	v_cvt_pk_bf16_f32 v140, v0, v1
	v_pk_mul_f32 v[0:1], v[58:59], s[58:59] op_sel_hi:[1,0]
	v_mov_b32_e32 v49, v32
	v_cvt_pk_bf16_f32 v141, v0, v1
	v_pk_mul_f32 v[0:1], v[76:77], s[58:59] op_sel_hi:[1,0]
	v_mov_b32_e32 v50, v32
	v_cvt_pk_bf16_f32 v142, v0, v1
	v_pk_mul_f32 v[0:1], v[72:73], s[58:59] op_sel_hi:[1,0]
	v_mov_b32_e32 v51, v32
	v_cvt_pk_bf16_f32 v143, v0, v1
	v_pk_mul_f32 v[0:1], v[68:69], s[58:59] op_sel_hi:[1,0]
	v_mov_b32_e32 v52, v32
	v_cvt_pk_bf16_f32 v144, v0, v1
	v_pk_mul_f32 v[0:1], v[62:63], s[58:59] op_sel_hi:[1,0]
	v_mov_b32_e32 v53, v32
	v_cvt_pk_bf16_f32 v145, v0, v1
	v_pk_mul_f32 v[0:1], v[46:47], s[58:59] op_sel_hi:[1,0]
	v_mov_b32_e32 v46, v32
	v_cvt_pk_bf16_f32 v146, v0, v1
	v_pk_mul_f32 v[0:1], v[54:55], s[58:59] op_sel_hi:[1,0]
	v_mov_b32_e32 v47, v32
	v_cvt_pk_bf16_f32 v147, v0, v1
	v_pk_mul_f32 v[0:1], v[44:45], s[58:59] op_sel_hi:[1,0]
	v_mov_b32_e32 v44, v32
	v_cvt_pk_bf16_f32 v148, v0, v1
	v_pk_mul_f32 v[0:1], v[64:65], s[58:59] op_sel_hi:[1,0]
	v_mov_b32_e32 v45, v32
	v_cvt_pk_bf16_f32 v149, v0, v1
	v_mov_b32_e32 v54, v32
	v_mov_b32_e32 v55, v32
	v_mov_b32_e32 v56, v32
	v_mov_b32_e32 v57, v32
	v_mov_b32_e32 v58, v32
	v_mov_b32_e32 v59, v32
	v_mov_b32_e32 v60, v32
	v_mov_b32_e32 v61, v32
	v_mov_b32_e32 v62, v32
	v_mov_b32_e32 v63, v32
	v_mov_b32_e32 v154, v32
	v_mov_b32_e32 v155, v32
	v_mov_b32_e32 v156, v32
	v_mov_b32_e32 v157, v32
	v_mov_b32_e32 v150, v32
	v_mov_b32_e32 v151, v32
	v_mov_b32_e32 v152, v32
	v_mov_b32_e32 v153, v32
	v_mov_b32_e32 v16, v32
	v_mov_b32_e32 v17, v32
	v_mov_b32_e32 v18, v32
	v_mov_b32_e32 v19, v32
	v_mov_b32_e32 v20, v32
	v_mov_b32_e32 v21, v32
	v_mov_b32_e32 v22, v32
	v_mov_b32_e32 v23, v32
	v_mov_b32_e32 v24, v32
	v_mov_b32_e32 v25, v32
	v_mov_b32_e32 v26, v32
	v_mov_b32_e32 v27, v32
	v_mov_b32_e32 v28, v32
	v_mov_b32_e32 v29, v32
	v_mov_b32_e32 v30, v32
	v_mov_b32_e32 v31, v32
	v_mov_b32_e32 v0, v32
	v_mov_b32_e32 v1, v32
	v_mov_b32_e32 v2, v32
	v_mov_b32_e32 v3, v32
	v_mov_b32_e32 v4, v32
	v_mov_b32_e32 v5, v32
	v_mov_b32_e32 v6, v32
	v_mov_b32_e32 v7, v32
	v_mov_b32_e32 v8, v32
	v_mov_b32_e32 v9, v32
	v_mov_b32_e32 v10, v32
	v_mov_b32_e32 v11, v32
	v_mov_b32_e32 v12, v32
	v_mov_b32_e32 v13, v32
	v_mov_b32_e32 v14, v32
	v_mov_b32_e32 v15, v32
	s_mov_b32 s69, s68
	s_mov_b32 s70, s68
	s_mov_b32 s71, s68
	s_mov_b32 s72, s68
	s_mov_b32 s73, s68
	s_mov_b32 s74, s68
	s_mov_b32 s75, s68
	s_mov_b32 s76, s68
	s_mov_b32 s77, s68
	s_mov_b32 s78, s68
	s_mov_b32 s79, s68
	s_mov_b32 s80, s68
	s_mov_b32 s81, s68
	s_mov_b32 s82, s68
	s_mov_b32 s83, s68
.LBB0_632:
	s_bitcmp1_b32 s12, 0
	s_cselect_b32 s14, 0, 0x5400
	s_cselect_b32 s13, 0x5400, 0
	s_add_i32 s14, s14, 0
	v_add3_u32 v234, s14, v220, v223
	global_load_dwordx4 v[158:161], v[194:195], off offset:-256
	global_load_dwordx4 v[162:165], v[194:195], off
	ds_read_b128 v[206:209], v234
	ds_read_b128 v[210:213], v234 offset:32
	ds_read_b128 v[226:229], v234 offset:64
	ds_read_b128 v[230:233], v234 offset:96
	s_waitcnt lgkmcnt(3)
	s_waitcnt lgkmcnt(2)
	s_waitcnt lgkmcnt(1)
	s_waitcnt lgkmcnt(0)
	v_add_u32_e32 v225, s14, v221
	v_mfma_f32_32x32x16_bf16 v[96:111], v[206:209], v[134:137], 0.5
	v_add3_u32 v225, v225, v222, v224
	s_add_i32 s12, s12, 1
	s_add_i32 s13, s13, 0
	s_add_i32 s14, s4, s12
	v_lshl_add_u64 v[194:195], v[194:195], 0, s[84:85]
	s_cmp_eq_u32 s14, 2
	v_mfma_f32_32x32x16_bf16 v[80:95], v[206:209], v[118:121], 0.5
	v_mfma_f32_32x32x16_bf16 v[96:111], v[210:213], v[138:141], v[96:111]
	v_mfma_f32_32x32x16_bf16 v[80:95], v[210:213], v[122:125], v[80:95]
	v_mfma_f32_32x32x16_bf16 v[96:111], v[226:229], v[142:145], v[96:111]
	v_mfma_f32_32x32x16_bf16 v[80:95], v[226:229], v[126:129], v[80:95]
	v_mfma_f32_32x32x16_bf16 v[96:111], v[230:233], v[146:149], v[96:111]
	v_mfma_f32_32x32x16_bf16 v[80:95], v[230:233], v[130:133], v[80:95]
	ds_read_b64_tr_b16 v[206:207], v225 offset:9216
	ds_read_b64_tr_b16 v[208:209], v225 offset:10752
	ds_read_b64_tr_b16 v[210:211], v225 offset:12288
	ds_read_b64_tr_b16 v[212:213], v225 offset:13824
	ds_read_b64_tr_b16 v[226:227], v225 offset:9280
	ds_read_b64_tr_b16 v[228:229], v225 offset:10816
	ds_read_b64_tr_b16 v[230:231], v225 offset:12352
	ds_read_b64_tr_b16 v[232:233], v225 offset:13888
	s_nop 2
	v_cvt_pknorm_i16_f32 v96, v96, v97
	v_cvt_pknorm_i16_f32 v97, v98, v99
	v_cvt_pknorm_i16_f32 v98, v100, v101
	v_cvt_pknorm_i16_f32 v99, v102, v103
	v_cvt_pknorm_i16_f32 v104, v104, v105
	v_cvt_pknorm_i16_f32 v105, v106, v107
	v_cvt_pknorm_i16_f32 v80, v80, v81
	v_cvt_pknorm_i16_f32 v81, v82, v83
	v_cvt_pknorm_i16_f32 v82, v84, v85
	v_cvt_pknorm_i16_f32 v83, v86, v87
	s_waitcnt lgkmcnt(6)
	v_mfma_f32_32x32x16_bf16 v[48:63], v[206:209], v[96:99], v[48:63]
	v_cvt_pknorm_i16_f32 v106, v108, v109
	v_cvt_pknorm_i16_f32 v107, v110, v111
	v_cvt_pknorm_i16_f32 v88, v88, v89
	v_cvt_pknorm_i16_f32 v89, v90, v91
	v_cvt_pknorm_i16_f32 v90, v92, v93
	v_cvt_pknorm_i16_f32 v91, v94, v95
	s_waitcnt lgkmcnt(2)
	v_mfma_f32_32x32x16_bf16 v[32:47], v[226:229], v[96:99], v[32:47]
	v_mfma_f32_32x32x16_bf16 v[16:31], v[206:209], v[80:83], v[16:31]
	v_mfma_f32_32x32x16_bf16 v[0:15], v[226:229], v[80:83], v[0:15]
	v_mfma_f32_16x16x32_bf16 v[100:103], v[114:117], v[96:99], v[150:153]
	v_mfma_f32_16x16x32_bf16 v[84:87], v[114:117], v[80:83], v[154:157]
	v_mfma_f32_32x32x16_bf16 v[48:63], v[210:213], v[104:107], v[48:63]
	s_waitcnt lgkmcnt(0)
	v_mfma_f32_32x32x16_bf16 v[32:47], v[230:233], v[104:107], v[32:47]
	v_mfma_f32_32x32x16_bf16 v[16:31], v[210:213], v[88:91], v[16:31]
	v_mfma_f32_32x32x16_bf16 v[0:15], v[230:233], v[88:91], v[0:15]
	ds_read_b128 v[206:209], v234 offset:4608
	ds_read_b128 v[210:213], v234 offset:4640
	ds_read_b128 v[226:229], v234 offset:4672
	ds_read_b128 v[230:233], v234 offset:4704
	s_waitcnt lgkmcnt(3)
	s_waitcnt lgkmcnt(2)
	s_waitcnt lgkmcnt(1)
	s_waitcnt lgkmcnt(0)
	v_mfma_f32_16x16x32_bf16 v[150:153], v[114:117], v[104:107], v[100:103]
	v_mfma_f32_16x16x32_bf16 v[154:157], v[114:117], v[88:91], v[84:87]
	v_mfma_f32_32x32x16_bf16 v[96:111], v[206:209], v[134:137], 0.5
	v_mfma_f32_32x32x16_bf16 v[80:95], v[206:209], v[118:121], 0.5
	ds_read_b64_tr_b16 v[64:65], v225 offset:15360
	ds_read_b64_tr_b16 v[66:67], v225 offset:16896
	ds_read_b64_tr_b16 v[68:69], v225 offset:18432
	ds_read_b64_tr_b16 v[70:71], v225 offset:19968
	ds_read_b64_tr_b16 v[72:73], v225 offset:15424
	ds_read_b64_tr_b16 v[74:75], v225 offset:16960
	ds_read_b64_tr_b16 v[76:77], v225 offset:18496
	ds_read_b64_tr_b16 v[78:79], v225 offset:20032
	v_mfma_f32_32x32x16_bf16 v[96:111], v[210:213], v[138:141], v[96:111]
	v_mfma_f32_32x32x16_bf16 v[80:95], v[210:213], v[122:125], v[80:95]
	v_mfma_f32_32x32x16_bf16 v[96:111], v[226:229], v[142:145], v[96:111]
	v_mfma_f32_32x32x16_bf16 v[80:95], v[226:229], v[126:129], v[80:95]
	v_mfma_f32_32x32x16_bf16 v[96:111], v[230:233], v[146:149], v[96:111]
	v_mfma_f32_32x32x16_bf16 v[80:95], v[230:233], v[130:133], v[80:95]
	s_nop 10
	v_cvt_pknorm_i16_f32 v96, v96, v97
	v_cvt_pknorm_i16_f32 v97, v98, v99
	v_cvt_pknorm_i16_f32 v98, v100, v101
	v_cvt_pknorm_i16_f32 v99, v102, v103
	v_cvt_pknorm_i16_f32 v104, v104, v105
	v_cvt_pknorm_i16_f32 v105, v106, v107
	v_cvt_pknorm_i16_f32 v106, v108, v109
	v_cvt_pknorm_i16_f32 v80, v80, v81
	v_cvt_pknorm_i16_f32 v81, v82, v83
	v_cvt_pknorm_i16_f32 v82, v84, v85
	v_cvt_pknorm_i16_f32 v83, v86, v87
	s_waitcnt lgkmcnt(6)
	v_mfma_f32_32x32x16_bf16 v[48:63], v[64:67], v[96:99], v[48:63]
	v_cvt_pknorm_i16_f32 v107, v110, v111
	v_cvt_pknorm_i16_f32 v88, v88, v89
	v_cvt_pknorm_i16_f32 v89, v90, v91
	v_cvt_pknorm_i16_f32 v90, v92, v93
	v_cvt_pknorm_i16_f32 v91, v94, v95
	s_waitcnt lgkmcnt(2)
	v_mfma_f32_32x32x16_bf16 v[32:47], v[72:75], v[96:99], v[32:47]
	v_mfma_f32_32x32x16_bf16 v[16:31], v[64:67], v[80:83], v[16:31]
	v_add3_u32 v64, s13, v217, v218
	v_add3_u32 v65, s13, v219, v218
	s_waitcnt vmcnt(1)
	ds_write_b128 v64, v[158:161]
	s_waitcnt vmcnt(0)
	ds_write_b128 v65, v[162:165] offset:9216
	s_waitcnt lgkmcnt(0)
	s_barrier
	v_mfma_f32_32x32x16_bf16 v[0:15], v[72:75], v[80:83], v[0:15]
	v_mfma_f32_16x16x32_bf16 v[100:103], v[114:117], v[96:99], v[150:153]
	v_mfma_f32_32x32x16_bf16 v[48:63], v[68:71], v[104:107], v[48:63]
	v_mfma_f32_32x32x16_bf16 v[32:47], v[76:79], v[104:107], v[32:47]
	v_mfma_f32_16x16x32_bf16 v[84:87], v[114:117], v[80:83], v[154:157]
	v_mfma_f32_32x32x16_bf16 v[16:31], v[68:71], v[88:91], v[16:31]
	v_mfma_f32_32x32x16_bf16 v[0:15], v[76:79], v[88:91], v[0:15]
	v_mfma_f32_16x16x32_bf16 v[150:153], v[114:117], v[104:107], v[100:103]
	v_mfma_f32_16x16x32_bf16 v[154:157], v[114:117], v[88:91], v[84:87]
	s_cbranch_scc0 .LBB0_632
	v_add3_u32 v194, s13, v220, v223
	v_mov_b64_e32 v[64:65], s[68:69]
	ds_read_b128 v[158:161], v194
	v_mov_b64_e32 v[66:67], s[70:71]
	v_mov_b64_e32 v[68:69], s[72:73]
	v_mov_b64_e32 v[70:71], s[74:75]
	v_mov_b64_e32 v[72:73], s[76:77]
	v_mov_b64_e32 v[74:75], s[78:79]
	v_mov_b64_e32 v[76:77], s[80:81]
	v_mov_b64_e32 v[78:79], s[82:83]
	ds_read_b128 v[162:165], v194 offset:32
	ds_read_b128 v[206:209], v194 offset:64
	ds_read_b128 v[210:213], v194 offset:96
	s_waitcnt lgkmcnt(3)
	s_waitcnt lgkmcnt(2)
	v_mfma_f32_32x32x16_bf16 v[96:111], v[158:161], v[134:137], v[64:79]
	s_waitcnt lgkmcnt(1)
	s_waitcnt lgkmcnt(0)
	v_mfma_f32_32x32x16_bf16 v[80:95], v[158:161], v[118:121], v[64:79]
	v_add_u32_e32 v158, s13, v221
	v_add3_u32 v195, v158, v222, v224
	ds_read_b64_tr_b16 v[158:159], v195 offset:9216
	ds_read_b64_tr_b16 v[160:161], v195 offset:10752
	v_mfma_f32_32x32x16_bf16 v[96:111], v[162:165], v[138:141], v[96:111]
	v_mfma_f32_32x32x16_bf16 v[80:95], v[162:165], v[122:125], v[80:95]
	v_mfma_f32_32x32x16_bf16 v[96:111], v[206:209], v[142:145], v[96:111]
	v_mfma_f32_32x32x16_bf16 v[80:95], v[206:209], v[126:129], v[80:95]
	v_mfma_f32_32x32x16_bf16 v[96:111], v[210:213], v[146:149], v[96:111]
	v_mfma_f32_32x32x16_bf16 v[80:95], v[210:213], v[130:133], v[80:95]
	s_nop 10
	v_cvt_pknorm_i16_f32 v96, v96, v97
	v_cvt_pknorm_i16_f32 v97, v98, v99
	v_cvt_pknorm_i16_f32 v98, v100, v101
	v_cvt_pknorm_i16_f32 v99, v102, v103
	ds_read_b64_tr_b16 v[102:103], v195 offset:10816
	ds_read_b64_tr_b16 v[100:101], v195 offset:9280
	ds_read_b64_tr_b16 v[162:163], v195 offset:12288
	ds_read_b64_tr_b16 v[164:165], v195 offset:13824
	v_cvt_pknorm_i16_f32 v104, v104, v105
	v_cvt_pknorm_i16_f32 v206, v80, v81
	v_cvt_pknorm_i16_f32 v207, v82, v83
	v_cvt_pknorm_i16_f32 v208, v84, v85
	v_cvt_pknorm_i16_f32 v209, v86, v87
	s_waitcnt lgkmcnt(4)
	v_mfma_f32_32x32x16_bf16 v[48:63], v[158:161], v[96:99], v[48:63]
	v_cvt_pknorm_i16_f32 v105, v106, v107
	v_cvt_pknorm_i16_f32 v106, v108, v109
	v_cvt_pknorm_i16_f32 v107, v110, v111
	ds_read_b64_tr_b16 v[110:111], v195 offset:13888
	ds_read_b64_tr_b16 v[108:109], v195 offset:12352
	s_waitcnt lgkmcnt(4)
	v_mfma_f32_32x32x16_bf16 v[32:47], v[100:103], v[96:99], v[32:47]
	v_mfma_f32_32x32x16_bf16 v[16:31], v[158:161], v[206:209], v[16:31]
	v_cvt_pknorm_i16_f32 v158, v88, v89
	v_cvt_pknorm_i16_f32 v159, v90, v91
	v_cvt_pknorm_i16_f32 v160, v92, v93
	v_cvt_pknorm_i16_f32 v161, v94, v95
	v_mfma_f32_32x32x16_bf16 v[0:15], v[100:103], v[206:209], v[0:15]
	s_waitcnt lgkmcnt(2)
	v_mfma_f32_32x32x16_bf16 v[48:63], v[162:165], v[104:107], v[48:63]
	s_waitcnt lgkmcnt(0)
	v_mfma_f32_32x32x16_bf16 v[32:47], v[108:111], v[104:107], v[32:47]
	v_mfma_f32_32x32x16_bf16 v[16:31], v[162:165], v[158:161], v[16:31]
	v_mfma_f32_32x32x16_bf16 v[0:15], v[108:111], v[158:161], v[0:15]
	ds_read_b128 v[100:103], v194 offset:4608
	ds_read_b128 v[108:111], v194 offset:4640
	ds_read_b128 v[162:165], v194 offset:4672
	ds_read_b128 v[210:213], v194 offset:4704
	s_waitcnt lgkmcnt(3)
	s_waitcnt lgkmcnt(2)
	s_waitcnt lgkmcnt(1)
	s_waitcnt lgkmcnt(0)
	v_mfma_f32_32x32x16_bf16 v[80:95], v[100:103], v[134:137], v[64:79]
	v_mfma_f32_32x32x16_bf16 v[64:79], v[100:103], v[118:121], v[64:79]
	ds_read_b64_tr_b16 v[100:101], v195 offset:15360
	ds_read_b64_tr_b16 v[102:103], v195 offset:16896
	v_mfma_f32_32x32x16_bf16 v[80:95], v[108:111], v[138:141], v[80:95]
	v_mfma_f32_32x32x16_bf16 v[64:79], v[108:111], v[122:125], v[64:79]
	v_mfma_f32_32x32x16_bf16 v[80:95], v[162:165], v[142:145], v[80:95]
	v_mfma_f32_32x32x16_bf16 v[64:79], v[162:165], v[126:129], v[64:79]
	v_mfma_f32_32x32x16_bf16 v[80:95], v[210:213], v[146:149], v[80:95]
	v_mfma_f32_32x32x16_bf16 v[64:79], v[210:213], v[130:133], v[64:79]
	s_nop 10
	v_cvt_pknorm_i16_f32 v80, v80, v81
	v_cvt_pknorm_i16_f32 v81, v82, v83
	v_cvt_pknorm_i16_f32 v82, v84, v85
	v_cvt_pknorm_i16_f32 v83, v86, v87
	ds_read_b64_tr_b16 v[86:87], v195 offset:16960
	ds_read_b64_tr_b16 v[84:85], v195 offset:15424
	ds_read_b64_tr_b16 v[108:109], v195 offset:18432
	ds_read_b64_tr_b16 v[110:111], v195 offset:19968
	v_cvt_pknorm_i16_f32 v88, v88, v89
	v_cvt_pknorm_i16_f32 v64, v64, v65
	v_cvt_pknorm_i16_f32 v65, v66, v67
	v_cvt_pknorm_i16_f32 v66, v68, v69
	v_cvt_pknorm_i16_f32 v67, v70, v71
	v_cvt_pknorm_i16_f32 v89, v90, v91
	v_cvt_pknorm_i16_f32 v90, v92, v93
	s_waitcnt lgkmcnt(2)
	v_mfma_f32_32x32x16_bf16 v[0:15], v[84:87], v[64:67], v[0:15]
	v_cvt_pknorm_i16_f32 v91, v94, v95
	ds_read_b64_tr_b16 v[94:95], v195 offset:20032
	ds_read_b64_tr_b16 v[92:93], v195 offset:18496
	v_cvt_pknorm_i16_f32 v68, v72, v73
	v_cvt_pknorm_i16_f32 v69, v74, v75
	v_cvt_pknorm_i16_f32 v70, v76, v77
	v_cvt_pknorm_i16_f32 v71, v78, v79
	s_waitcnt lgkmcnt(0)
	v_mfma_f32_16x16x32_bf16 v[72:75], v[114:117], v[96:99], v[150:153]
	s_barrier
	v_mfma_f32_16x16x32_bf16 v[76:79], v[114:117], v[206:209], v[154:157]
	v_mfma_f32_32x32x16_bf16 v[48:63], v[100:103], v[80:83], v[48:63]
	v_mfma_f32_32x32x16_bf16 v[32:47], v[84:87], v[80:83], v[32:47]
	v_mfma_f32_32x32x16_bf16 v[16:31], v[100:103], v[64:67], v[16:31]
	v_mfma_f32_16x16x32_bf16 v[72:75], v[114:117], v[104:107], v[72:75]
	v_mfma_f32_16x16x32_bf16 v[76:79], v[114:117], v[158:161], v[76:79]
	v_mfma_f32_32x32x16_bf16 v[0:15], v[92:95], v[68:71], v[0:15]
	v_mfma_f32_16x16x32_bf16 v[72:75], v[114:117], v[80:83], v[72:75]
	v_mfma_f32_16x16x32_bf16 v[64:67], v[114:117], v[64:67], v[76:79]
	v_mfma_f32_32x32x16_bf16 v[48:63], v[108:111], v[88:91], v[48:63]
	v_mfma_f32_32x32x16_bf16 v[32:47], v[92:95], v[88:91], v[32:47]
	v_mfma_f32_32x32x16_bf16 v[16:31], v[108:111], v[68:71], v[16:31]
	v_mfma_f32_16x16x32_bf16 v[72:75], v[114:117], v[88:91], v[72:75]
	v_mfma_f32_16x16x32_bf16 v[64:67], v[114:117], v[68:71], v[64:67]
	s_setprio 0
	s_nop 6
	ds_bpermute_b32 v66, v181, v72
	ds_bpermute_b32 v67, v181, v73
	ds_bpermute_b32 v64, v181, v64
	ds_bpermute_b32 v65, v181, v65
	v_lshl_add_u64 v[150:151], v[192:193], 0, s[56:57]
	s_mov_b64 s[46:47], 0
	s_waitcnt lgkmcnt(2)
	v_cndmask_b32_e64 v66, v67, v66, s[40:41]
	v_div_scale_f32 v67, s[12:13], v66, v66, 1.0
	v_rcp_f32_e32 v68, v67
	s_waitcnt lgkmcnt(0)
	v_cndmask_b32_e64 v64, v65, v64, s[40:41]
	v_div_scale_f32 v65, s[12:13], v64, v64, 1.0
	v_fma_f32 v69, -v67, v68, 1.0
	v_fmac_f32_e32 v68, v69, v68
	v_div_scale_f32 v69, vcc, 1.0, v66, 1.0
	v_mul_f32_e32 v70, v69, v68
	v_fma_f32 v71, -v67, v70, v69
	v_fmac_f32_e32 v70, v71, v68
	v_fma_f32 v67, -v67, v70, v69
	v_div_fmas_f32 v67, v67, v68, v70
	v_div_fixup_f32 v66, v67, v66, 1.0
	v_rcp_f32_e32 v67, v65
	v_readlane_b32 s70, v255, 14
	s_mov_b32 s21, s20
	s_mov_b32 s71, s66
	v_fma_f32 v68, -v65, v67, 1.0
	v_fmac_f32_e32 v67, v68, v67
	v_div_scale_f32 v68, vcc, 1.0, v64, 1.0
	v_mul_f32_e32 v69, v68, v67
	v_fma_f32 v70, -v65, v69, v68
	v_fmac_f32_e32 v69, v70, v67
	v_fma_f32 v65, -v65, v69, v68
	v_div_fmas_f32 v65, v65, v67, v69
	v_div_fixup_f32 v64, v65, v64, 1.0
	v_pk_mul_f32 v[48:49], v[48:49], v[66:67] op_sel_hi:[1,0]
	v_pk_mul_f32 v[50:51], v[50:51], v[66:67] op_sel_hi:[1,0]
	v_pk_mul_f32 v[32:33], v[32:33], v[66:67] op_sel_hi:[1,0]
	v_pk_mul_f32 v[34:35], v[34:35], v[66:67] op_sel_hi:[1,0]
	v_pk_mul_f32 v[16:17], v[16:17], v[64:65] op_sel_hi:[1,0]
	v_pk_mul_f32 v[18:19], v[18:19], v[64:65] op_sel_hi:[1,0]
	v_pk_mul_f32 v[0:1], v[0:1], v[64:65] op_sel_hi:[1,0]
	v_pk_mul_f32 v[2:3], v[2:3], v[64:65] op_sel_hi:[1,0]
	v_cvt_pk_bf16_f32 v48, v48, v49
	v_cvt_pk_bf16_f32 v49, v50, v51
	v_lshl_add_u64 v[50:51], v[182:183], 1, v[192:193]
	v_cvt_pk_bf16_f32 v32, v32, v33
	v_cvt_pk_bf16_f32 v33, v34, v35
	v_cvt_pk_bf16_f32 v16, v16, v17
	v_cvt_pk_bf16_f32 v17, v18, v19
	v_cvt_pk_bf16_f32 v0, v0, v1
	v_cvt_pk_bf16_f32 v1, v2, v3
	global_store_dwordx2 v[50:51], v[48:49], off
	v_pk_mul_f32 v[48:49], v[52:53], v[66:67] op_sel_hi:[1,0]
	v_pk_mul_f32 v[52:53], v[54:55], v[66:67] op_sel_hi:[1,0]
	global_store_dwordx2 v[50:51], v[32:33], off offset:64
	v_pk_mul_f32 v[32:33], v[36:37], v[66:67] op_sel_hi:[1,0]
	v_pk_mul_f32 v[34:35], v[38:39], v[66:67] op_sel_hi:[1,0]
	global_store_dwordx2 v[50:51], v[16:17], off offset:128
	v_pk_mul_f32 v[16:17], v[20:21], v[64:65] op_sel_hi:[1,0]
	v_pk_mul_f32 v[18:19], v[22:23], v[64:65] op_sel_hi:[1,0]
	global_store_dwordx2 v[50:51], v[0:1], off offset:192
	v_pk_mul_f32 v[0:1], v[4:5], v[64:65] op_sel_hi:[1,0]
	v_pk_mul_f32 v[2:3], v[6:7], v[64:65] op_sel_hi:[1,0]
	v_cvt_pk_bf16_f32 v48, v48, v49
	v_cvt_pk_bf16_f32 v49, v52, v53
	v_cvt_pk_bf16_f32 v32, v32, v33
	v_cvt_pk_bf16_f32 v33, v34, v35
	v_cvt_pk_bf16_f32 v16, v16, v17
	v_cvt_pk_bf16_f32 v17, v18, v19
	v_cvt_pk_bf16_f32 v0, v0, v1
	v_cvt_pk_bf16_f32 v1, v2, v3
	global_store_dwordx2 v[50:51], v[48:49], off offset:16
	v_pk_mul_f32 v[48:49], v[56:57], v[66:67] op_sel_hi:[1,0]
	v_pk_mul_f32 v[52:53], v[58:59], v[66:67] op_sel_hi:[1,0]
	global_store_dwordx2 v[50:51], v[32:33], off offset:80
	v_pk_mul_f32 v[32:33], v[40:41], v[66:67] op_sel_hi:[1,0]
	v_pk_mul_f32 v[34:35], v[42:43], v[66:67] op_sel_hi:[1,0]
	global_store_dwordx2 v[50:51], v[16:17], off offset:144
	v_pk_mul_f32 v[16:17], v[24:25], v[64:65] op_sel_hi:[1,0]
	v_pk_mul_f32 v[18:19], v[26:27], v[64:65] op_sel_hi:[1,0]
	global_store_dwordx2 v[50:51], v[0:1], off offset:208
	v_pk_mul_f32 v[0:1], v[8:9], v[64:65] op_sel_hi:[1,0]
	v_pk_mul_f32 v[2:3], v[10:11], v[64:65] op_sel_hi:[1,0]
	v_cvt_pk_bf16_f32 v48, v48, v49
	v_cvt_pk_bf16_f32 v49, v52, v53
	v_cvt_pk_bf16_f32 v32, v32, v33
	v_cvt_pk_bf16_f32 v33, v34, v35
	v_cvt_pk_bf16_f32 v16, v16, v17
	v_cvt_pk_bf16_f32 v17, v18, v19
	v_cvt_pk_bf16_f32 v0, v0, v1
	v_cvt_pk_bf16_f32 v1, v2, v3
	global_store_dwordx2 v[50:51], v[48:49], off offset:32
	v_pk_mul_f32 v[48:49], v[60:61], v[66:67] op_sel_hi:[1,0]
	v_pk_mul_f32 v[52:53], v[62:63], v[66:67] op_sel_hi:[1,0]
	global_store_dwordx2 v[50:51], v[32:33], off offset:96
	v_pk_mul_f32 v[32:33], v[44:45], v[66:67] op_sel_hi:[1,0]
	v_pk_mul_f32 v[34:35], v[46:47], v[66:67] op_sel_hi:[1,0]
	global_store_dwordx2 v[50:51], v[16:17], off offset:160
	v_pk_mul_f32 v[16:17], v[28:29], v[64:65] op_sel_hi:[1,0]
	v_pk_mul_f32 v[18:19], v[30:31], v[64:65] op_sel_hi:[1,0]
	global_store_dwordx2 v[50:51], v[0:1], off offset:224
	v_pk_mul_f32 v[0:1], v[12:13], v[64:65] op_sel_hi:[1,0]
	v_cvt_pk_bf16_f32 v48, v48, v49
	v_cvt_pk_bf16_f32 v49, v52, v53
	v_cvt_pk_bf16_f32 v32, v32, v33
	v_cvt_pk_bf16_f32 v33, v34, v35
	v_cvt_pk_bf16_f32 v16, v16, v17
	v_cvt_pk_bf16_f32 v17, v18, v19
	v_cvt_pk_bf16_f32 v0, v0, v1
	v_pk_mul_f32 v[2:3], v[14:15], v[64:65] op_sel_hi:[1,0]
	global_store_dwordx2 v[50:51], v[48:49], off offset:48
	global_store_dwordx2 v[50:51], v[32:33], off offset:112
	global_store_dwordx2 v[50:51], v[16:17], off offset:176

.LBB0_641:
	v_pk_mul_f32 v[0:1], v[24:25], s[60:61] op_sel_hi:[1,0]
	s_lshl_b32 s14, s12, 6
	v_cvt_pk_bf16_f32 v118, v0, v1
	v_pk_mul_f32 v[0:1], v[28:29], s[60:61] op_sel_hi:[1,0]
	s_and_b64 s[12:13], s[70:71], exec
	v_cvt_pk_bf16_f32 v119, v0, v1
	v_pk_mul_f32 v[0:1], v[20:21], s[60:61] op_sel_hi:[1,0]
	s_cselect_b32 s4, -2, 0xffffffbe
	v_cvt_pk_bf16_f32 v120, v0, v1
	v_pk_mul_f32 v[0:1], v[22:23], s[60:61] op_sel_hi:[1,0]
	s_lshl_b32 s14, s14, 1
	v_cvt_pk_bf16_f32 v121, v0, v1
	v_pk_mul_f32 v[0:1], v[30:31], s[60:61] op_sel_hi:[1,0]
	s_mul_i32 s12, s2, 0x220000
	v_cvt_pk_bf16_f32 v122, v0, v1
	v_pk_mul_f32 v[0:1], v[34:35], s[60:61] op_sel_hi:[1,0]
	s_and_b32 s14, s14, 0x180
	v_cvt_pk_bf16_f32 v123, v0, v1
	v_pk_mul_f32 v[0:1], v[26:27], s[60:61] op_sel_hi:[1,0]
	s_mul_hi_i32 s13, s2, 0x220000
	v_cvt_pk_bf16_f32 v124, v0, v1
	v_pk_mul_f32 v[0:1], v[32:33], s[60:61] op_sel_hi:[1,0]
	s_or_b32 s12, s12, s14
	v_cvt_pk_bf16_f32 v125, v0, v1
	v_pk_mul_f32 v[0:1], v[38:39], s[60:61] op_sel_hi:[1,0]
	s_mov_b32 s2, 1
	v_cvt_pk_bf16_f32 v126, v0, v1
	v_pk_mul_f32 v[0:1], v[44:45], s[60:61] op_sel_hi:[1,0]
	v_lshl_add_u64 v[152:153], v[190:191], 0, s[12:13]
	v_cvt_pk_bf16_f32 v127, v0, v1
	v_pk_mul_f32 v[0:1], v[36:37], s[60:61] op_sel_hi:[1,0]
	s_nop 0
	v_cvt_pk_bf16_f32 v128, v0, v1
	v_pk_mul_f32 v[0:1], v[40:41], s[60:61] op_sel_hi:[1,0]
	s_nop 0
	v_cvt_pk_bf16_f32 v129, v0, v1
	v_pk_mul_f32 v[0:1], v[46:47], s[60:61] op_sel_hi:[1,0]
	s_nop 0
	v_cvt_pk_bf16_f32 v130, v0, v1
	v_pk_mul_f32 v[0:1], v[50:51], s[60:61] op_sel_hi:[1,0]
	s_nop 0
	v_cvt_pk_bf16_f32 v131, v0, v1
	v_pk_mul_f32 v[0:1], v[42:43], s[60:61] op_sel_hi:[1,0]
	s_nop 0
	v_cvt_pk_bf16_f32 v132, v0, v1
	v_pk_mul_f32 v[0:1], v[48:49], s[60:61] op_sel_hi:[1,0]
	s_nop 0
	v_cvt_pk_bf16_f32 v133, v0, v1
	v_mov_b32_e32 v0, 0
	v_mov_b32_e32 v1, v0
	v_mov_b32_e32 v2, v0
	v_mov_b32_e32 v3, v0
	v_mov_b32_e32 v4, v0
	v_mov_b32_e32 v5, v0
	v_mov_b32_e32 v6, v0
	v_mov_b32_e32 v7, v0
	v_mov_b32_e32 v8, v0
	v_mov_b32_e32 v9, v0
	v_mov_b32_e32 v10, v0
	v_mov_b32_e32 v11, v0
	v_mov_b32_e32 v12, v0
	v_mov_b32_e32 v13, v0
	v_mov_b32_e32 v14, v0
	v_mov_b32_e32 v15, v0
	v_mov_b32_e32 v32, v0
	v_mov_b32_e32 v33, v0
	v_mov_b32_e32 v34, v0
	v_mov_b32_e32 v35, v0
	v_mov_b32_e32 v36, v0
	v_mov_b32_e32 v37, v0
	v_mov_b32_e32 v38, v0
	v_mov_b32_e32 v39, v0
	v_mov_b32_e32 v40, v0
	v_mov_b32_e32 v41, v0
	v_mov_b32_e32 v42, v0
	v_mov_b32_e32 v43, v0
	v_mov_b32_e32 v44, v0
	v_mov_b32_e32 v45, v0
	v_mov_b32_e32 v46, v0
	v_mov_b32_e32 v47, v0
	v_mov_b32_e32 v138, v0
	v_mov_b32_e32 v139, v0
	v_mov_b32_e32 v140, v0
	v_mov_b32_e32 v141, v0
	v_mov_b32_e32 v134, v0
	v_mov_b32_e32 v135, v0
	v_mov_b32_e32 v136, v0
	v_mov_b32_e32 v137, v0
	v_mov_b32_e32 v48, v0
	v_mov_b32_e32 v49, v0
	v_mov_b32_e32 v50, v0
	v_mov_b32_e32 v51, v0
	v_mov_b32_e32 v52, v0
	v_mov_b32_e32 v53, v0
	v_mov_b32_e32 v54, v0
	v_mov_b32_e32 v55, v0
	v_mov_b32_e32 v56, v0
	v_mov_b32_e32 v57, v0
	v_mov_b32_e32 v58, v0
	v_mov_b32_e32 v59, v0
	v_mov_b32_e32 v60, v0
	v_mov_b32_e32 v61, v0
	v_mov_b32_e32 v62, v0
	v_mov_b32_e32 v63, v0
	v_mov_b32_e32 v16, v0
	v_mov_b32_e32 v17, v0
	v_mov_b32_e32 v18, v0
	v_mov_b32_e32 v19, v0
	v_mov_b32_e32 v20, v0
	v_mov_b32_e32 v21, v0
	v_mov_b32_e32 v22, v0
	v_mov_b32_e32 v23, v0
	v_mov_b32_e32 v24, v0
	v_mov_b32_e32 v25, v0
	v_mov_b32_e32 v26, v0
	v_mov_b32_e32 v27, v0
	v_mov_b32_e32 v28, v0
	v_mov_b32_e32 v29, v0
	v_mov_b32_e32 v30, v0
	v_mov_b32_e32 v31, v0
	s_mov_b32 s69, s68
	s_mov_b32 s70, s68
	s_mov_b32 s71, s68
	s_mov_b32 s72, s68
	s_mov_b32 s73, s68
	s_mov_b32 s74, s68
	s_mov_b32 s75, s68
	s_mov_b32 s76, s68
	s_mov_b32 s77, s68
	s_mov_b32 s78, s68
	s_mov_b32 s79, s68
	s_mov_b32 s80, s68
	s_mov_b32 s81, s68
	s_mov_b32 s82, s68
	s_mov_b32 s83, s68
.LBB0_642:
	s_bitcmp1_b32 s2, 0
	s_mov_b32 s14, 0x2200000
	s_cselect_b32 s13, 0, 0x5400
	v_add_co_u32_e32 v64, vcc, s14, v152
	s_cselect_b32 s12, 0x5400, 0
	s_add_i32 s13, s13, 0
	global_load_dwordx4 v[142:145], v[152:153], off
	v_addc_co_u32_e32 v65, vcc, 0, v153, vcc
	global_load_dwordx4 v[146:149], v[64:65], off
	v_add3_u32 v206, s13, v220, v223
	ds_read_b128 v[80:83], v206
	ds_read_b128 v[84:87], v206 offset:32
	ds_read_b128 v[154:157], v206 offset:64
	ds_read_b128 v[158:161], v206 offset:96
	s_waitcnt lgkmcnt(3)
	s_waitcnt lgkmcnt(2)
	s_waitcnt lgkmcnt(1)
	s_waitcnt lgkmcnt(0)
	v_add_u32_e32 v112, s13, v221
	v_mfma_f32_32x32x16_bf16 v[96:111], v[80:83], v[126:129], 0.5
	v_add3_u32 v112, v112, v222, v224
	s_add_i32 s2, s2, 1
	s_add_i32 s12, s12, 0
	s_add_i32 s13, s4, s2
	v_lshl_add_u64 v[152:153], v[152:153], 0, s[84:85]
	s_cmp_eq_u32 s13, 2
	v_mfma_f32_32x32x16_bf16 v[96:111], v[84:87], v[130:133], v[96:111]
	v_mfma_f32_32x32x16_bf16 v[80:95], v[154:157], v[118:121], 0.5
	s_nop 10
	v_cvt_pknorm_i16_f32 v96, v96, v97
	v_cvt_pknorm_i16_f32 v97, v98, v99
	v_cvt_pknorm_i16_f32 v98, v100, v101
	v_cvt_pknorm_i16_f32 v99, v102, v103
	v_cvt_pknorm_i16_f32 v104, v104, v105
	v_cvt_pknorm_i16_f32 v105, v106, v107
	v_cvt_pknorm_i16_f32 v106, v108, v109
	v_mfma_f32_32x32x16_bf16 v[80:95], v[158:161], v[122:125], v[80:95]
	ds_read_b64_tr_b16 v[154:155], v112 offset:9216
	ds_read_b64_tr_b16 v[156:157], v112 offset:10752
	ds_read_b64_tr_b16 v[158:159], v112 offset:12288
	ds_read_b64_tr_b16 v[160:161], v112 offset:13824
	ds_read_b64_tr_b16 v[162:163], v112 offset:9280
	ds_read_b64_tr_b16 v[164:165], v112 offset:10816
	ds_read_b64_tr_b16 v[192:193], v112 offset:12352
	ds_read_b64_tr_b16 v[194:195], v112 offset:13888
	v_cvt_pknorm_i16_f32 v107, v110, v111
	s_nop 2
	v_cvt_pknorm_i16_f32 v80, v80, v81
	v_cvt_pknorm_i16_f32 v81, v82, v83
	v_cvt_pknorm_i16_f32 v82, v84, v85
	v_cvt_pknorm_i16_f32 v83, v86, v87
	s_waitcnt lgkmcnt(6)
	v_mfma_f32_32x32x16_bf16 v[32:47], v[154:157], v[96:99], v[32:47]
	v_cvt_pknorm_i16_f32 v88, v88, v89
	v_cvt_pknorm_i16_f32 v89, v90, v91
	v_cvt_pknorm_i16_f32 v90, v92, v93
	v_cvt_pknorm_i16_f32 v91, v94, v95
	v_mfma_f32_32x32x16_bf16 v[48:63], v[154:157], v[80:83], v[48:63]
	s_waitcnt lgkmcnt(2)
	v_mfma_f32_32x32x16_bf16 v[0:15], v[162:165], v[96:99], v[0:15]
	v_mfma_f32_16x16x32_bf16 v[84:87], v[114:117], v[80:83], v[138:141]
	v_mfma_f32_16x16x32_bf16 v[100:103], v[114:117], v[96:99], v[134:137]
	v_mfma_f32_32x32x16_bf16 v[32:47], v[158:161], v[104:107], v[32:47]
	v_mfma_f32_16x16x32_bf16 v[138:141], v[114:117], v[88:91], v[84:87]
	v_mfma_f32_32x32x16_bf16 v[48:63], v[158:161], v[88:91], v[48:63]
	v_mfma_f32_32x32x16_bf16 v[16:31], v[162:165], v[80:83], v[16:31]
	ds_read_b128 v[80:83], v206 offset:4608
	s_nop 1
	ds_read_b128 v[84:87], v206 offset:4640
	ds_read_b128 v[154:157], v206 offset:4672
	ds_read_b128 v[158:161], v206 offset:4704
	s_waitcnt lgkmcnt(3)
	s_waitcnt lgkmcnt(2)
	s_waitcnt lgkmcnt(1)
	s_waitcnt lgkmcnt(0)
	v_mfma_f32_16x16x32_bf16 v[134:137], v[114:117], v[104:107], v[100:103]
	v_mfma_f32_32x32x16_bf16 v[0:15], v[192:195], v[104:107], v[0:15]
	v_mfma_f32_32x32x16_bf16 v[96:111], v[80:83], v[126:129], 0.5
	v_mfma_f32_32x32x16_bf16 v[16:31], v[192:195], v[88:91], v[16:31]
	v_mfma_f32_32x32x16_bf16 v[96:111], v[84:87], v[130:133], v[96:111]
	v_mfma_f32_32x32x16_bf16 v[80:95], v[154:157], v[118:121], 0.5
	ds_read_b64_tr_b16 v[64:65], v112 offset:15360
	ds_read_b64_tr_b16 v[66:67], v112 offset:16896
	ds_read_b64_tr_b16 v[68:69], v112 offset:18432
	ds_read_b64_tr_b16 v[70:71], v112 offset:19968
	ds_read_b64_tr_b16 v[72:73], v112 offset:15424
	ds_read_b64_tr_b16 v[74:75], v112 offset:16960
	ds_read_b64_tr_b16 v[76:77], v112 offset:18496
	ds_read_b64_tr_b16 v[78:79], v112 offset:20032
	v_cvt_pknorm_i16_f32 v96, v96, v97
	v_cvt_pknorm_i16_f32 v97, v98, v99
	v_cvt_pknorm_i16_f32 v98, v100, v101
	v_cvt_pknorm_i16_f32 v99, v102, v103
	v_cvt_pknorm_i16_f32 v104, v104, v105
	v_cvt_pknorm_i16_f32 v105, v106, v107
	v_mfma_f32_32x32x16_bf16 v[80:95], v[158:161], v[122:125], v[80:95]
	v_cvt_pknorm_i16_f32 v106, v108, v109
	v_cvt_pknorm_i16_f32 v107, v110, v111
	s_waitcnt lgkmcnt(6)
	v_mfma_f32_32x32x16_bf16 v[32:47], v[64:67], v[96:99], v[32:47]
	s_nop 7
	v_cvt_pknorm_i16_f32 v80, v80, v81
	v_cvt_pknorm_i16_f32 v81, v82, v83
	v_cvt_pknorm_i16_f32 v82, v84, v85
	v_cvt_pknorm_i16_f32 v83, v86, v87
	v_cvt_pknorm_i16_f32 v88, v88, v89
	v_cvt_pknorm_i16_f32 v89, v90, v91
	v_cvt_pknorm_i16_f32 v90, v92, v93
	s_waitcnt lgkmcnt(2)
	v_mfma_f32_32x32x16_bf16 v[0:15], v[72:75], v[96:99], v[0:15]
	v_cvt_pknorm_i16_f32 v91, v94, v95
	v_mfma_f32_32x32x16_bf16 v[48:63], v[64:67], v[80:83], v[48:63]
	v_add3_u32 v64, s12, v217, v218
	v_add3_u32 v65, s12, v219, v218
	s_waitcnt vmcnt(1)
	ds_write_b128 v64, v[142:145]
	s_waitcnt vmcnt(0)
	ds_write_b128 v65, v[146:149] offset:9216
	s_waitcnt lgkmcnt(0)
	s_barrier
	v_mfma_f32_32x32x16_bf16 v[16:31], v[72:75], v[80:83], v[16:31]
	v_mfma_f32_16x16x32_bf16 v[100:103], v[114:117], v[96:99], v[134:137]
	v_mfma_f32_32x32x16_bf16 v[32:47], v[68:71], v[104:107], v[32:47]
	v_mfma_f32_32x32x16_bf16 v[0:15], v[76:79], v[104:107], v[0:15]
	v_mfma_f32_16x16x32_bf16 v[84:87], v[114:117], v[80:83], v[138:141]
	v_mfma_f32_32x32x16_bf16 v[48:63], v[68:71], v[88:91], v[48:63]
	v_mfma_f32_32x32x16_bf16 v[16:31], v[76:79], v[88:91], v[16:31]
	v_mfma_f32_16x16x32_bf16 v[134:137], v[114:117], v[104:107], v[100:103]
	v_mfma_f32_16x16x32_bf16 v[138:141], v[114:117], v[88:91], v[84:87]
	s_cbranch_scc0 .LBB0_642
	v_add3_u32 v112, s12, v220, v223
	v_mov_b64_e32 v[64:65], s[68:69]
	ds_read_b128 v[80:83], v112
	v_mov_b64_e32 v[66:67], s[70:71]
	v_mov_b64_e32 v[68:69], s[72:73]
	v_mov_b64_e32 v[70:71], s[74:75]
	v_mov_b64_e32 v[72:73], s[76:77]
	v_mov_b64_e32 v[74:75], s[78:79]
	v_mov_b64_e32 v[76:77], s[80:81]
	v_mov_b64_e32 v[78:79], s[82:83]
	ds_read_b128 v[84:87], v112 offset:32
	ds_read_b128 v[142:145], v112 offset:64
	ds_read_b128 v[146:149], v112 offset:96
	s_waitcnt lgkmcnt(3)
	s_waitcnt lgkmcnt(2)
	v_mfma_f32_32x32x16_bf16 v[96:111], v[80:83], v[126:129], v[64:79]
	s_waitcnt lgkmcnt(1)
	s_waitcnt lgkmcnt(0)
	v_mfma_f32_32x32x16_bf16 v[96:111], v[84:87], v[130:133], v[96:111]
	v_mfma_f32_32x32x16_bf16 v[80:95], v[142:145], v[118:121], v[64:79]
	v_add_u32_e32 v142, s12, v221
	v_add3_u32 v160, v142, v222, v224
	ds_read_b64_tr_b16 v[142:143], v160 offset:9216
	ds_read_b64_tr_b16 v[144:145], v160 offset:10752
	s_nop 6
	v_cvt_pknorm_i16_f32 v96, v96, v97
	v_cvt_pknorm_i16_f32 v97, v98, v99
	v_cvt_pknorm_i16_f32 v98, v100, v101
	v_cvt_pknorm_i16_f32 v99, v102, v103
	v_mfma_f32_32x32x16_bf16 v[80:95], v[146:149], v[122:125], v[80:95]
	ds_read_b64_tr_b16 v[102:103], v160 offset:10816
	ds_read_b64_tr_b16 v[100:101], v160 offset:9280
	ds_read_b64_tr_b16 v[146:147], v160 offset:12288
	ds_read_b64_tr_b16 v[148:149], v160 offset:13824
	v_cvt_pknorm_i16_f32 v104, v104, v105
	v_cvt_pknorm_i16_f32 v105, v106, v107
	v_cvt_pknorm_i16_f32 v106, v108, v109
	v_cvt_pknorm_i16_f32 v107, v110, v111
	ds_read_b64_tr_b16 v[110:111], v160 offset:13888
	ds_read_b64_tr_b16 v[108:109], v160 offset:12352
	s_nop 1
	v_cvt_pknorm_i16_f32 v152, v80, v81
	v_cvt_pknorm_i16_f32 v153, v82, v83
	v_cvt_pknorm_i16_f32 v154, v84, v85
	v_cvt_pknorm_i16_f32 v155, v86, v87
	s_waitcnt lgkmcnt(6)
	v_mfma_f32_32x32x16_bf16 v[32:47], v[142:145], v[96:99], v[32:47]
	s_waitcnt lgkmcnt(4)
	v_mfma_f32_32x32x16_bf16 v[0:15], v[100:103], v[96:99], v[0:15]
	v_mfma_f32_32x32x16_bf16 v[48:63], v[142:145], v[152:155], v[48:63]
	v_cvt_pknorm_i16_f32 v142, v88, v89
	v_cvt_pknorm_i16_f32 v143, v90, v91
	v_cvt_pknorm_i16_f32 v144, v92, v93
	v_cvt_pknorm_i16_f32 v145, v94, v95
	v_mfma_f32_32x32x16_bf16 v[16:31], v[100:103], v[152:155], v[16:31]
	s_waitcnt lgkmcnt(2)
	v_mfma_f32_32x32x16_bf16 v[32:47], v[146:149], v[104:107], v[32:47]
	s_waitcnt lgkmcnt(0)
	v_mfma_f32_32x32x16_bf16 v[0:15], v[108:111], v[104:107], v[0:15]
	v_mfma_f32_32x32x16_bf16 v[48:63], v[146:149], v[142:145], v[48:63]
	v_mfma_f32_32x32x16_bf16 v[16:31], v[108:111], v[142:145], v[16:31]
	ds_read_b128 v[100:103], v112 offset:4608
	ds_read_b128 v[108:111], v112 offset:4640
	ds_read_b128 v[146:149], v112 offset:4672
	ds_read_b128 v[156:159], v112 offset:4704
	s_waitcnt lgkmcnt(3)
	s_waitcnt lgkmcnt(2)
	s_waitcnt lgkmcnt(1)
	s_waitcnt lgkmcnt(0)
	v_mfma_f32_32x32x16_bf16 v[80:95], v[100:103], v[126:129], v[64:79]
	ds_read_b64_tr_b16 v[100:101], v160 offset:15360
	ds_read_b64_tr_b16 v[102:103], v160 offset:16896
	v_mfma_f32_32x32x16_bf16 v[80:95], v[108:111], v[130:133], v[80:95]
	v_mfma_f32_32x32x16_bf16 v[64:79], v[146:149], v[118:121], v[64:79]
	s_nop 10
	v_cvt_pknorm_i16_f32 v80, v80, v81
	v_cvt_pknorm_i16_f32 v81, v82, v83
	v_cvt_pknorm_i16_f32 v82, v84, v85
	v_cvt_pknorm_i16_f32 v83, v86, v87
	ds_read_b64_tr_b16 v[86:87], v160 offset:16960
	ds_read_b64_tr_b16 v[84:85], v160 offset:15424
	ds_read_b64_tr_b16 v[108:109], v160 offset:18432
	ds_read_b64_tr_b16 v[110:111], v160 offset:19968
	v_cvt_pknorm_i16_f32 v88, v88, v89
	v_mfma_f32_32x32x16_bf16 v[64:79], v[156:159], v[122:125], v[64:79]
	v_cvt_pknorm_i16_f32 v89, v90, v91
	v_cvt_pknorm_i16_f32 v90, v92, v93
	v_cvt_pknorm_i16_f32 v91, v94, v95
	ds_read_b64_tr_b16 v[94:95], v160 offset:20032
	ds_read_b64_tr_b16 v[92:93], v160 offset:18496
	s_load_dword s2, s[6:7], 0x180
	s_waitcnt lgkmcnt(0)
	s_barrier
	v_mfma_f32_32x32x16_bf16 v[0:15], v[84:87], v[80:83], v[0:15]
	s_nop 2
	v_cvt_pknorm_i16_f32 v64, v64, v65
	v_cvt_pknorm_i16_f32 v65, v66, v67
	v_cvt_pknorm_i16_f32 v66, v68, v69
	v_cvt_pknorm_i16_f32 v68, v72, v73
	v_cvt_pknorm_i16_f32 v69, v74, v75
	v_cvt_pknorm_i16_f32 v67, v70, v71
	v_cvt_pknorm_i16_f32 v70, v76, v77
	v_mfma_f32_16x16x32_bf16 v[72:75], v[114:117], v[96:99], v[134:137]
	v_cvt_pknorm_i16_f32 v71, v78, v79
	v_mfma_f32_16x16x32_bf16 v[76:79], v[114:117], v[152:155], v[138:141]
	v_mfma_f32_16x16x32_bf16 v[72:75], v[114:117], v[104:107], v[72:75]
	v_mfma_f32_32x32x16_bf16 v[32:47], v[100:103], v[80:83], v[32:47]
	v_mfma_f32_32x32x16_bf16 v[0:15], v[92:95], v[88:91], v[0:15]
	v_mfma_f32_32x32x16_bf16 v[48:63], v[100:103], v[64:67], v[48:63]
	v_mfma_f32_32x32x16_bf16 v[16:31], v[84:87], v[64:67], v[16:31]
	v_mfma_f32_16x16x32_bf16 v[76:79], v[114:117], v[142:145], v[76:79]
	v_mfma_f32_16x16x32_bf16 v[72:75], v[114:117], v[80:83], v[72:75]
	v_mfma_f32_16x16x32_bf16 v[64:67], v[114:117], v[64:67], v[76:79]
	v_mfma_f32_16x16x32_bf16 v[72:75], v[114:117], v[88:91], v[72:75]
	v_mfma_f32_32x32x16_bf16 v[32:47], v[108:111], v[88:91], v[32:47]
	s_nop 6
	v_sub_f32_e64 v74, 1.0, s2
	v_mfma_f32_32x32x16_bf16 v[48:63], v[108:111], v[68:71], v[48:63]
	v_mfma_f32_16x16x32_bf16 v[64:67], v[114:117], v[68:71], v[64:67]
	v_mfma_f32_32x32x16_bf16 v[16:31], v[92:95], v[68:71], v[16:31]
	s_setprio 0
	s_nop 5
	ds_bpermute_b32 v66, v181, v72
	ds_bpermute_b32 v67, v181, v73
	ds_bpermute_b32 v64, v181, v64
	ds_bpermute_b32 v65, v181, v65
	v_readlane_b32 s70, v255, 14
	s_mov_b32 s21, s20
	s_waitcnt lgkmcnt(2)
	v_cndmask_b32_e64 v66, v67, v66, s[40:41]
	v_div_scale_f32 v67, s[12:13], v66, v66, 1.0
	v_rcp_f32_e32 v68, v67
	s_waitcnt lgkmcnt(0)
	v_cndmask_b32_e64 v64, v65, v64, s[40:41]
	v_div_scale_f32 v65, s[12:13], v64, v64, 1.0
	v_fma_f32 v69, -v67, v68, 1.0
	v_fmac_f32_e32 v68, v69, v68
	v_div_scale_f32 v69, vcc, 1.0, v66, 1.0
	v_mul_f32_e32 v70, v69, v68
	v_fma_f32 v71, -v67, v70, v69
	v_fmac_f32_e32 v70, v71, v68
	v_fma_f32 v67, -v67, v70, v69
	v_div_fmas_f32 v67, v67, v68, v70
	v_div_fixup_f32 v66, v67, v66, 1.0
	v_rcp_f32_e32 v67, v65
	s_mov_b32 s71, s66
	v_fma_f32 v68, -v65, v67, 1.0
	v_fmac_f32_e32 v67, v68, v67
	v_div_scale_f32 v68, vcc, 1.0, v64, 1.0
	v_mul_f32_e32 v69, v68, v67
	v_fma_f32 v70, -v65, v69, v68
	v_fmac_f32_e32 v69, v70, v67
	v_fma_f32 v65, -v65, v69, v68
	v_div_fmas_f32 v65, v65, v67, v69
	global_load_dwordx4 v[68:71], v[186:187], off
	v_div_fixup_f32 v72, v65, v64, 1.0
	v_pk_mul_f32 v[30:31], v[30:31], v[72:73] op_sel_hi:[1,0]
	v_pk_mul_f32 v[18:19], v[18:19], v[72:73] op_sel_hi:[1,0]
	v_pk_mul_f32 v[30:31], v[166:167], v[30:31]
	v_pk_mul_f32 v[18:19], v[166:167], v[18:19]
	v_pk_fma_f32 v[14:15], v[14:15], v[66:67], v[30:31] op_sel_hi:[1,0,1] neg_lo:[0,0,1] neg_hi:[0,0,1]
	v_pk_mul_f32 v[30:31], v[50:51], v[72:73] op_sel_hi:[1,0]
	v_pk_fma_f32 v[18:19], v[2:3], v[66:67], v[18:19] op_sel_hi:[1,0,1] neg_lo:[0,0,1] neg_hi:[0,0,1]
	v_pk_mul_f32 v[30:31], v[166:167], v[30:31]
	v_pk_mul_f32 v[2:3], v[16:17], v[72:73] op_sel_hi:[1,0]
	v_pk_fma_f32 v[30:31], v[34:35], v[66:67], v[30:31] op_sel_hi:[1,0,1] neg_lo:[0,0,1] neg_hi:[0,0,1]
	v_pk_mul_f32 v[34:35], v[48:49], v[72:73] op_sel_hi:[1,0]
	v_mul_f32_e32 v48, v31, v31
	v_pk_mul_f32 v[34:35], v[166:167], v[34:35]
	v_pk_mul_f32 v[2:3], v[166:167], v[2:3]
	v_pk_fma_f32 v[32:33], v[32:33], v[66:67], v[34:35] op_sel_hi:[1,0,1] neg_lo:[0,0,1] neg_hi:[0,0,1]
	v_pk_fma_f32 v[16:17], v[0:1], v[66:67], v[2:3] op_sel_hi:[1,0,1] neg_lo:[0,0,1] neg_hi:[0,0,1]
	v_mul_f32_e32 v34, v33, v33
	v_pk_fma_f32 v[34:35], v[32:33], v[32:33], v[34:35] op_sel_hi:[1,1,0]
	v_mul_f32_e32 v2, v17, v17
	v_pk_fma_f32 v[34:35], v[30:31], v[30:31], v[34:35]
	v_lshl_add_u64 v[64:65], v[182:183], 1, v[150:151]
	v_pk_add_f32 v[34:35], v[48:49], v[34:35] op_sel_hi:[0,1]
	v_pk_mul_f32 v[48:49], v[54:55], v[72:73] op_sel_hi:[1,0]
	s_nop 0
	v_pk_mul_f32 v[48:49], v[166:167], v[48:49]
	s_nop 0
	v_pk_fma_f32 v[38:39], v[38:39], v[66:67], v[48:49] op_sel_hi:[1,0,1] neg_lo:[0,0,1] neg_hi:[0,0,1]
	v_pk_mul_f32 v[48:49], v[52:53], v[72:73] op_sel_hi:[1,0]
	s_nop 0
	v_pk_mul_f32 v[48:49], v[166:167], v[48:49]
	s_nop 0
	v_pk_fma_f32 v[36:37], v[36:37], v[66:67], v[48:49] op_sel_hi:[1,0,1] neg_lo:[0,0,1] neg_hi:[0,0,1]
	s_nop 0
	v_pk_fma_f32 v[34:35], v[36:37], v[36:37], v[34:35]
	v_mul_f32_e32 v48, v37, v37
	v_pk_add_f32 v[34:35], v[48:49], v[34:35] op_sel_hi:[0,1]
	v_pk_fma_f32 v[34:35], v[38:39], v[38:39], v[34:35]
	v_mul_f32_e32 v48, v39, v39
	v_pk_add_f32 v[34:35], v[48:49], v[34:35] op_sel_hi:[0,1]
	v_pk_mul_f32 v[48:49], v[58:59], v[72:73] op_sel_hi:[1,0]
	s_nop 0
	v_pk_mul_f32 v[48:49], v[166:167], v[48:49]
	s_nop 0
	v_pk_fma_f32 v[42:43], v[42:43], v[66:67], v[48:49] op_sel_hi:[1,0,1] neg_lo:[0,0,1] neg_hi:[0,0,1]
	v_pk_mul_f32 v[48:49], v[56:57], v[72:73] op_sel_hi:[1,0]
	s_nop 0
	v_pk_mul_f32 v[48:49], v[166:167], v[48:49]
	s_nop 0
	v_pk_fma_f32 v[40:41], v[40:41], v[66:67], v[48:49] op_sel_hi:[1,0,1] neg_lo:[0,0,1] neg_hi:[0,0,1]
	s_nop 0
	v_pk_fma_f32 v[34:35], v[40:41], v[40:41], v[34:35]
	v_mul_f32_e32 v48, v41, v41
	v_pk_add_f32 v[34:35], v[48:49], v[34:35] op_sel_hi:[0,1]
	v_pk_fma_f32 v[34:35], v[42:43], v[42:43], v[34:35]
	v_mul_f32_e32 v48, v43, v43
	v_pk_add_f32 v[34:35], v[48:49], v[34:35] op_sel_hi:[0,1]
	v_pk_mul_f32 v[48:49], v[62:63], v[72:73] op_sel_hi:[1,0]
	s_nop 0
	v_pk_mul_f32 v[48:49], v[166:167], v[48:49]
	s_nop 0
	v_pk_fma_f32 v[46:47], v[46:47], v[66:67], v[48:49] op_sel_hi:[1,0,1] neg_lo:[0,0,1] neg_hi:[0,0,1]
	v_pk_mul_f32 v[48:49], v[60:61], v[72:73] op_sel_hi:[1,0]
	s_nop 0
	v_pk_mul_f32 v[48:49], v[166:167], v[48:49]
	s_nop 0
	v_pk_fma_f32 v[44:45], v[44:45], v[66:67], v[48:49] op_sel_hi:[1,0,1] neg_lo:[0,0,1] neg_hi:[0,0,1]
	s_nop 0
	v_pk_fma_f32 v[34:35], v[44:45], v[44:45], v[34:35]
	v_mul_f32_e32 v48, v45, v45
	v_pk_add_f32 v[34:35], v[48:49], v[34:35] op_sel_hi:[0,1]
	v_pk_fma_f32 v[34:35], v[46:47], v[46:47], v[34:35]
	v_mul_f32_e32 v48, v47, v47
	v_pk_add_f32 v[34:35], v[48:49], v[34:35] op_sel_hi:[0,1]
	v_pk_fma_f32 v[0:1], v[16:17], v[16:17], v[34:35]
	s_nop 0
	v_pk_add_f32 v[0:1], v[2:3], v[0:1] op_sel_hi:[0,1]
	v_pk_fma_f32 v[0:1], v[18:19], v[18:19], v[0:1]
	v_mul_f32_e32 v2, v19, v19
	v_pk_add_f32 v[0:1], v[2:3], v[0:1] op_sel_hi:[0,1]
	v_pk_mul_f32 v[2:3], v[22:23], v[72:73] op_sel_hi:[1,0]
	s_nop 0
	v_pk_mul_f32 v[2:3], v[166:167], v[2:3]
	s_nop 0
	v_pk_fma_f32 v[6:7], v[6:7], v[66:67], v[2:3] op_sel_hi:[1,0,1] neg_lo:[0,0,1] neg_hi:[0,0,1]
	v_pk_mul_f32 v[2:3], v[20:21], v[72:73] op_sel_hi:[1,0]
	s_nop 0
	v_pk_mul_f32 v[2:3], v[166:167], v[2:3]
	s_nop 0
	v_pk_fma_f32 v[4:5], v[4:5], v[66:67], v[2:3] op_sel_hi:[1,0,1] neg_lo:[0,0,1] neg_hi:[0,0,1]
	s_nop 0
	v_pk_fma_f32 v[0:1], v[4:5], v[4:5], v[0:1]
	v_mul_f32_e32 v2, v5, v5
	v_pk_add_f32 v[0:1], v[2:3], v[0:1] op_sel_hi:[0,1]
	v_pk_fma_f32 v[0:1], v[6:7], v[6:7], v[0:1]
	v_mul_f32_e32 v2, v7, v7
	v_pk_add_f32 v[0:1], v[2:3], v[0:1] op_sel_hi:[0,1]
	v_pk_mul_f32 v[2:3], v[26:27], v[72:73] op_sel_hi:[1,0]
	s_nop 0
	v_pk_mul_f32 v[2:3], v[166:167], v[2:3]
	s_nop 0
	v_pk_fma_f32 v[10:11], v[10:11], v[66:67], v[2:3] op_sel_hi:[1,0,1] neg_lo:[0,0,1] neg_hi:[0,0,1]
	v_pk_mul_f32 v[2:3], v[24:25], v[72:73] op_sel_hi:[1,0]
	s_nop 0
	v_pk_mul_f32 v[2:3], v[166:167], v[2:3]
	s_nop 0
	v_pk_fma_f32 v[8:9], v[8:9], v[66:67], v[2:3] op_sel_hi:[1,0,1] neg_lo:[0,0,1] neg_hi:[0,0,1]
	s_nop 0
	v_pk_fma_f32 v[0:1], v[8:9], v[8:9], v[0:1]
	v_mul_f32_e32 v2, v9, v9
	v_pk_add_f32 v[0:1], v[2:3], v[0:1] op_sel_hi:[0,1]
	v_pk_fma_f32 v[0:1], v[10:11], v[10:11], v[0:1]
	v_mul_f32_e32 v2, v11, v11
	v_pk_add_f32 v[0:1], v[2:3], v[0:1] op_sel_hi:[0,1]
	v_pk_mul_f32 v[2:3], v[28:29], v[72:73] op_sel_hi:[1,0]
	s_nop 0
	v_pk_mul_f32 v[2:3], v[166:167], v[2:3]
	s_nop 0
	v_pk_fma_f32 v[12:13], v[12:13], v[66:67], v[2:3] op_sel_hi:[1,0,1] neg_lo:[0,0,1] neg_hi:[0,0,1]
	s_nop 0
	v_pk_fma_f32 v[0:1], v[12:13], v[12:13], v[0:1]
	v_mul_f32_e32 v2, v13, v13
	v_pk_add_f32 v[0:1], v[2:3], v[0:1] op_sel_hi:[0,1]
	v_pk_fma_f32 v[0:1], v[14:15], v[14:15], v[0:1]
	v_mul_f32_e32 v2, v15, v15
	v_pk_add_f32 v[0:1], v[2:3], v[0:1] op_sel_hi:[0,1]
	v_mov_b32_e32 v1, v0
	s_nop 1
	v_permlane32_swap_b32_e32 v0, v1
	v_add_f32_e32 v0, v0, v1
	v_fmamk_f32 v0, v0, 0x3c800000, v196
	v_cmp_gt_f32_e32 vcc, s35, v0
	v_mul_f32_e32 v1, 0x4b800000, v0
	s_nop 0
	v_cndmask_b32_e32 v0, v0, v1, vcc
	v_rsq_f32_e32 v0, v0
	s_nop 0
	v_mul_f32_e32 v1, 0x45800000, v0
	v_cndmask_b32_e32 v0, v0, v1, vcc
	v_mul_f32_e32 v20, v74, v0
	v_pk_mul_f32 v[0:1], v[32:33], v[20:21] op_sel_hi:[1,0]
	v_pk_mul_f32 v[2:3], v[30:31], v[20:21] op_sel_hi:[1,0]
	s_waitcnt vmcnt(0)
	v_pk_mul_f32 v[0:1], v[68:69], v[0:1]
	v_pk_mul_f32 v[2:3], v[70:71], v[2:3]
	v_cvt_pk_bf16_f32 v0, v0, v1
	v_cvt_pk_bf16_f32 v1, v2, v3
	global_store_dwordx2 v[64:65], v[0:1], off
	global_load_dwordx4 v[0:3], v[186:187], off offset:32
	v_pk_mul_f32 v[22:23], v[36:37], v[20:21] op_sel_hi:[1,0]
	v_pk_mul_f32 v[16:17], v[16:17], v[20:21] op_sel_hi:[1,0]
	v_pk_mul_f32 v[4:5], v[4:5], v[20:21] op_sel_hi:[1,0]
	s_waitcnt vmcnt(0)
	v_pk_mul_f32 v[0:1], v[0:1], v[22:23]
	v_pk_mul_f32 v[22:23], v[38:39], v[20:21] op_sel_hi:[1,0]
	v_cvt_pk_bf16_f32 v0, v0, v1
	v_pk_mul_f32 v[2:3], v[2:3], v[22:23]
	v_pk_mul_f32 v[22:23], v[40:41], v[20:21] op_sel_hi:[1,0]
	v_cvt_pk_bf16_f32 v1, v2, v3
	global_store_dwordx2 v[64:65], v[0:1], off offset:16
	global_load_dwordx4 v[0:3], v[186:187], off offset:64
	s_waitcnt vmcnt(0)
	v_pk_mul_f32 v[0:1], v[0:1], v[22:23]
	v_pk_mul_f32 v[22:23], v[42:43], v[20:21] op_sel_hi:[1,0]
	v_cvt_pk_bf16_f32 v0, v0, v1
	v_pk_mul_f32 v[2:3], v[2:3], v[22:23]
	v_pk_mul_f32 v[22:23], v[44:45], v[20:21] op_sel_hi:[1,0]
	v_cvt_pk_bf16_f32 v1, v2, v3
	global_store_dwordx2 v[64:65], v[0:1], off offset:32
	global_load_dwordx4 v[0:3], v[186:187], off offset:96
	s_waitcnt vmcnt(0)
	v_pk_mul_f32 v[0:1], v[0:1], v[22:23]
	v_pk_mul_f32 v[22:23], v[46:47], v[20:21] op_sel_hi:[1,0]
	v_cvt_pk_bf16_f32 v0, v0, v1
	v_pk_mul_f32 v[2:3], v[2:3], v[22:23]
	s_nop 0
	v_cvt_pk_bf16_f32 v1, v2, v3
	global_store_dwordx2 v[64:65], v[0:1], off offset:48
	global_load_dwordx4 v[0:3], v[186:187], off offset:128
	s_waitcnt vmcnt(0)
	v_pk_mul_f32 v[0:1], v[0:1], v[16:17]
	v_pk_mul_f32 v[16:17], v[18:19], v[20:21] op_sel_hi:[1,0]
	v_cvt_pk_bf16_f32 v0, v0, v1
	v_pk_mul_f32 v[2:3], v[2:3], v[16:17]
	s_nop 0
	v_cvt_pk_bf16_f32 v1, v2, v3
	global_store_dwordx2 v[64:65], v[0:1], off offset:64
	global_load_dwordx4 v[0:3], v[186:187], off offset:160
	s_waitcnt vmcnt(0)
	v_pk_mul_f32 v[0:1], v[0:1], v[4:5]
	v_pk_mul_f32 v[4:5], v[6:7], v[20:21] op_sel_hi:[1,0]
	v_cvt_pk_bf16_f32 v0, v0, v1
	v_pk_mul_f32 v[2:3], v[2:3], v[4:5]
	v_pk_mul_f32 v[4:5], v[8:9], v[20:21] op_sel_hi:[1,0]
	v_cvt_pk_bf16_f32 v1, v2, v3
	global_store_dwordx2 v[64:65], v[0:1], off offset:80
	global_load_dwordx4 v[0:3], v[186:187], off offset:192
	s_waitcnt vmcnt(0)
	v_pk_mul_f32 v[0:1], v[4:5], v[0:1]
	v_pk_mul_f32 v[4:5], v[10:11], v[20:21] op_sel_hi:[1,0]
	v_cvt_pk_bf16_f32 v0, v0, v1
	v_pk_mul_f32 v[2:3], v[4:5], v[2:3]
	v_pk_mul_f32 v[4:5], v[12:13], v[20:21] op_sel_hi:[1,0]
	v_cvt_pk_bf16_f32 v1, v2, v3
	global_store_dwordx2 v[64:65], v[0:1], off offset:96
	global_load_dwordx4 v[0:3], v[186:187], off offset:224
	s_waitcnt vmcnt(0)
	v_pk_mul_f32 v[0:1], v[4:5], v[0:1]
	v_pk_mul_f32 v[4:5], v[14:15], v[20:21] op_sel_hi:[1,0]
	v_cvt_pk_bf16_f32 v0, v0, v1
	v_pk_mul_f32 v[2:3], v[4:5], v[2:3]
	s_branch .LBB0_617
